# MoE down-GEMM scatter epilogue de-serialised: all 16 slot-table loads issued up front, one wait, then 8 convert+store groups (4 layer copies)
# speedup vs baseline: 1.0055x; 1.0017x over previous
.LBB0_1070:
	v_lshl_or_b32 v136, s67, 8, v148
	v_ashrrev_i32_e32 v137, 31, v136
	v_add_u32_e32 v192, s49, v138
	v_ashrrev_i32_e32 v193, 31, v192
	v_lshlrev_b64 v[192:193], 2, v[192:193]
	v_lshl_add_u64 v[194:195], s[12:13], 0, v[192:193]
	v_lshl_add_u64 v[192:193], s[8:9], 0, v[192:193]
	global_load_dword v160, v[192:193], off
	global_load_dword v162, v[194:195], off
	global_load_dword v164, v[192:193], off offset:64
	global_load_dword v166, v[194:195], off offset:64
	global_load_dword v168, v[192:193], off offset:128
	global_load_dword v170, v[194:195], off offset:128
	global_load_dword v172, v[192:193], off offset:192
	global_load_dword v174, v[194:195], off offset:192
	global_load_dword v176, v[192:193], off offset:512
	global_load_dword v178, v[194:195], off offset:512
	global_load_dword v180, v[192:193], off offset:576
	global_load_dword v182, v[194:195], off offset:576
	global_load_dword v184, v[192:193], off offset:640
	global_load_dword v186, v[194:195], off offset:640
	global_load_dword v188, v[192:193], off offset:704
	global_load_dword v190, v[194:195], off offset:704
	s_waitcnt vmcnt(0)
	v_cmp_gt_i32_e32 vcc, s52, v138
	s_and_saveexec_b64 s[36:37], vcc
	s_cbranch_execz .LBB0_1072
	v_mov_b32_e32 v152, 0
	v_mov_b32_e32 v153, 0
	v_mov_b32_e32 v154, 0
	v_mov_b32_e32 v155, 0
	v_ashrrev_i32_e32 v161, 31, v160
	v_mul_f32_e32 v162, 0x41800000, v162
	v_pk_mul_f32 v[112:113], v[112:113], v[162:163] op_sel_hi:[1,0]
	v_pk_mul_f32 v[116:117], v[116:117], v[162:163] op_sel_hi:[1,0]
	v_pk_mul_f32 v[120:121], v[120:121], v[162:163] op_sel_hi:[1,0]
	v_pk_mul_f32 v[124:125], v[124:125], v[162:163] op_sel_hi:[1,0]
	v_cvt_pk_fp8_f32 v152, v112, v113
	v_cvt_pk_fp8_f32 v153, v116, v117
	v_cvt_pk_fp8_f32 v154, v120, v121
	v_cvt_pk_fp8_f32 v155, v124, v125
	v_pk_mul_f32 v[114:115], v[114:115], v[162:163] op_sel_hi:[1,0]
	v_pk_mul_f32 v[118:119], v[118:119], v[162:163] op_sel_hi:[1,0]
	v_pk_mul_f32 v[122:123], v[122:123], v[162:163] op_sel_hi:[1,0]
	v_pk_mul_f32 v[126:127], v[126:127], v[162:163] op_sel_hi:[1,0]
	v_cvt_pk_fp8_f32 v152, v114, v115 op_sel:[0,0,1]
	v_cvt_pk_fp8_f32 v153, v118, v119 op_sel:[0,0,1]
	v_cvt_pk_fp8_f32 v154, v122, v123 op_sel:[0,0,1]
	v_cvt_pk_fp8_f32 v155, v126, v127 op_sel:[0,0,1]
	v_lshlrev_b64 v[112:113], 10, v[160:161]
	v_lshl_add_u64 v[112:113], s[6:7], 0, v[112:113]
	v_lshl_add_u64 v[112:113], v[112:113], 0, v[136:137]
	global_store_dwordx4 v[112:113], v[152:155], off
.LBB0_1072:
	s_or_b64 exec, exec, s[36:37]
	v_or_b32_e32 v112, 16, v138
	v_cmp_gt_i32_e32 vcc, s52, v112
	s_and_saveexec_b64 s[36:37], vcc
	s_cbranch_execz .LBB0_1074
	v_mov_b32_e32 v112, 0
	v_mov_b32_e32 v113, 0
	v_mov_b32_e32 v114, 0
	v_mov_b32_e32 v115, 0
	v_ashrrev_i32_e32 v165, 31, v164
	v_mul_f32_e32 v166, 0x41800000, v166
	v_pk_mul_f32 v[96:97], v[96:97], v[166:167] op_sel_hi:[1,0]
	v_pk_mul_f32 v[100:101], v[100:101], v[166:167] op_sel_hi:[1,0]
	v_pk_mul_f32 v[104:105], v[104:105], v[166:167] op_sel_hi:[1,0]
	v_pk_mul_f32 v[108:109], v[108:109], v[166:167] op_sel_hi:[1,0]
	v_cvt_pk_fp8_f32 v112, v96, v97
	v_cvt_pk_fp8_f32 v113, v100, v101
	v_cvt_pk_fp8_f32 v114, v104, v105
	v_cvt_pk_fp8_f32 v115, v108, v109
	v_pk_mul_f32 v[98:99], v[98:99], v[166:167] op_sel_hi:[1,0]
	v_pk_mul_f32 v[102:103], v[102:103], v[166:167] op_sel_hi:[1,0]
	v_pk_mul_f32 v[106:107], v[106:107], v[166:167] op_sel_hi:[1,0]
	v_pk_mul_f32 v[110:111], v[110:111], v[166:167] op_sel_hi:[1,0]
	v_cvt_pk_fp8_f32 v112, v98, v99 op_sel:[0,0,1]
	v_cvt_pk_fp8_f32 v113, v102, v103 op_sel:[0,0,1]
	v_cvt_pk_fp8_f32 v114, v106, v107 op_sel:[0,0,1]
	v_cvt_pk_fp8_f32 v115, v110, v111 op_sel:[0,0,1]
	v_lshlrev_b64 v[96:97], 10, v[164:165]
	v_lshl_add_u64 v[96:97], s[6:7], 0, v[96:97]
	v_lshl_add_u64 v[96:97], v[96:97], 0, v[136:137]
	global_store_dwordx4 v[96:97], v[112:115], off
.LBB0_1074:
	s_or_b64 exec, exec, s[36:37]
	v_or_b32_e32 v96, 32, v138
	v_cmp_gt_i32_e32 vcc, s52, v96
	s_and_saveexec_b64 s[36:37], vcc
	s_cbranch_execz .LBB0_1076
	v_mov_b32_e32 v96, 0
	v_mov_b32_e32 v97, 0
	v_mov_b32_e32 v98, 0
	v_mov_b32_e32 v99, 0
	v_ashrrev_i32_e32 v169, 31, v168
	v_mul_f32_e32 v170, 0x41800000, v170
	v_pk_mul_f32 v[80:81], v[80:81], v[170:171] op_sel_hi:[1,0]
	v_pk_mul_f32 v[84:85], v[84:85], v[170:171] op_sel_hi:[1,0]
	v_pk_mul_f32 v[88:89], v[88:89], v[170:171] op_sel_hi:[1,0]
	v_pk_mul_f32 v[92:93], v[92:93], v[170:171] op_sel_hi:[1,0]
	v_cvt_pk_fp8_f32 v96, v80, v81
	v_cvt_pk_fp8_f32 v97, v84, v85
	v_cvt_pk_fp8_f32 v98, v88, v89
	v_cvt_pk_fp8_f32 v99, v92, v93
	v_pk_mul_f32 v[82:83], v[82:83], v[170:171] op_sel_hi:[1,0]
	v_pk_mul_f32 v[86:87], v[86:87], v[170:171] op_sel_hi:[1,0]
	v_pk_mul_f32 v[90:91], v[90:91], v[170:171] op_sel_hi:[1,0]
	v_pk_mul_f32 v[94:95], v[94:95], v[170:171] op_sel_hi:[1,0]
	v_cvt_pk_fp8_f32 v96, v82, v83 op_sel:[0,0,1]
	v_cvt_pk_fp8_f32 v97, v86, v87 op_sel:[0,0,1]
	v_cvt_pk_fp8_f32 v98, v90, v91 op_sel:[0,0,1]
	v_cvt_pk_fp8_f32 v99, v94, v95 op_sel:[0,0,1]
	v_lshlrev_b64 v[80:81], 10, v[168:169]
	v_lshl_add_u64 v[80:81], s[6:7], 0, v[80:81]
	v_lshl_add_u64 v[80:81], v[80:81], 0, v[136:137]
	global_store_dwordx4 v[80:81], v[96:99], off
.LBB0_1076:
	s_or_b64 exec, exec, s[36:37]
	v_or_b32_e32 v80, 48, v138
	v_cmp_gt_i32_e32 vcc, s52, v80
	s_and_saveexec_b64 s[36:37], vcc
	s_cbranch_execz .LBB0_1078
	v_mov_b32_e32 v80, 0
	v_mov_b32_e32 v81, 0
	v_mov_b32_e32 v82, 0
	v_mov_b32_e32 v83, 0
	v_ashrrev_i32_e32 v173, 31, v172
	v_mul_f32_e32 v174, 0x41800000, v174
	v_pk_mul_f32 v[64:65], v[64:65], v[174:175] op_sel_hi:[1,0]
	v_pk_mul_f32 v[68:69], v[68:69], v[174:175] op_sel_hi:[1,0]
	v_pk_mul_f32 v[72:73], v[72:73], v[174:175] op_sel_hi:[1,0]
	v_pk_mul_f32 v[76:77], v[76:77], v[174:175] op_sel_hi:[1,0]
	v_cvt_pk_fp8_f32 v80, v64, v65
	v_cvt_pk_fp8_f32 v81, v68, v69
	v_cvt_pk_fp8_f32 v82, v72, v73
	v_cvt_pk_fp8_f32 v83, v76, v77
	v_pk_mul_f32 v[66:67], v[66:67], v[174:175] op_sel_hi:[1,0]
	v_pk_mul_f32 v[70:71], v[70:71], v[174:175] op_sel_hi:[1,0]
	v_pk_mul_f32 v[74:75], v[74:75], v[174:175] op_sel_hi:[1,0]
	v_pk_mul_f32 v[78:79], v[78:79], v[174:175] op_sel_hi:[1,0]
	v_cvt_pk_fp8_f32 v80, v66, v67 op_sel:[0,0,1]
	v_cvt_pk_fp8_f32 v81, v70, v71 op_sel:[0,0,1]
	v_cvt_pk_fp8_f32 v82, v74, v75 op_sel:[0,0,1]
	v_cvt_pk_fp8_f32 v83, v78, v79 op_sel:[0,0,1]
	v_lshlrev_b64 v[64:65], 10, v[172:173]
	v_lshl_add_u64 v[64:65], s[6:7], 0, v[64:65]
	v_lshl_add_u64 v[64:65], v[64:65], 0, v[136:137]
	global_store_dwordx4 v[64:65], v[80:83], off
.LBB0_1078:
	s_or_b64 exec, exec, s[36:37]
	v_add_u32_e32 v64, 0x80, v138
	v_cmp_gt_i32_e32 vcc, s52, v64
	s_and_saveexec_b64 s[36:37], vcc
	s_cbranch_execz .LBB0_1080
	v_mov_b32_e32 v64, 0
	v_mov_b32_e32 v65, 0
	v_mov_b32_e32 v66, 0
	v_mov_b32_e32 v67, 0
	v_ashrrev_i32_e32 v177, 31, v176
	v_mul_f32_e32 v178, 0x41800000, v178
	v_pk_mul_f32 v[48:49], v[48:49], v[178:179] op_sel_hi:[1,0]
	v_pk_mul_f32 v[52:53], v[52:53], v[178:179] op_sel_hi:[1,0]
	v_pk_mul_f32 v[56:57], v[56:57], v[178:179] op_sel_hi:[1,0]
	v_pk_mul_f32 v[60:61], v[60:61], v[178:179] op_sel_hi:[1,0]
	v_cvt_pk_fp8_f32 v64, v48, v49
	v_cvt_pk_fp8_f32 v65, v52, v53
	v_cvt_pk_fp8_f32 v66, v56, v57
	v_cvt_pk_fp8_f32 v67, v60, v61
	v_pk_mul_f32 v[50:51], v[50:51], v[178:179] op_sel_hi:[1,0]
	v_pk_mul_f32 v[54:55], v[54:55], v[178:179] op_sel_hi:[1,0]
	v_pk_mul_f32 v[58:59], v[58:59], v[178:179] op_sel_hi:[1,0]
	v_pk_mul_f32 v[62:63], v[62:63], v[178:179] op_sel_hi:[1,0]
	v_cvt_pk_fp8_f32 v64, v50, v51 op_sel:[0,0,1]
	v_cvt_pk_fp8_f32 v65, v54, v55 op_sel:[0,0,1]
	v_cvt_pk_fp8_f32 v66, v58, v59 op_sel:[0,0,1]
	v_cvt_pk_fp8_f32 v67, v62, v63 op_sel:[0,0,1]
	v_lshlrev_b64 v[48:49], 10, v[176:177]
	v_lshl_add_u64 v[48:49], s[6:7], 0, v[48:49]
	v_lshl_add_u64 v[48:49], v[48:49], 0, v[136:137]
	global_store_dwordx4 v[48:49], v[64:67], off
.LBB0_1080:
	s_or_b64 exec, exec, s[36:37]
	v_add_u32_e32 v48, 0x90, v138
	v_cmp_gt_i32_e32 vcc, s52, v48
	s_and_saveexec_b64 s[36:37], vcc
	s_cbranch_execz .LBB0_1082
	v_mov_b32_e32 v48, 0
	v_mov_b32_e32 v49, 0
	v_mov_b32_e32 v50, 0
	v_mov_b32_e32 v51, 0
	v_ashrrev_i32_e32 v181, 31, v180
	v_mul_f32_e32 v182, 0x41800000, v182
	v_pk_mul_f32 v[32:33], v[32:33], v[182:183] op_sel_hi:[1,0]
	v_pk_mul_f32 v[36:37], v[36:37], v[182:183] op_sel_hi:[1,0]
	v_pk_mul_f32 v[40:41], v[40:41], v[182:183] op_sel_hi:[1,0]
	v_pk_mul_f32 v[44:45], v[44:45], v[182:183] op_sel_hi:[1,0]
	v_cvt_pk_fp8_f32 v48, v32, v33
	v_cvt_pk_fp8_f32 v49, v36, v37
	v_cvt_pk_fp8_f32 v50, v40, v41
	v_cvt_pk_fp8_f32 v51, v44, v45
	v_pk_mul_f32 v[34:35], v[34:35], v[182:183] op_sel_hi:[1,0]
	v_pk_mul_f32 v[38:39], v[38:39], v[182:183] op_sel_hi:[1,0]
	v_pk_mul_f32 v[42:43], v[42:43], v[182:183] op_sel_hi:[1,0]
	v_pk_mul_f32 v[46:47], v[46:47], v[182:183] op_sel_hi:[1,0]
	v_cvt_pk_fp8_f32 v48, v34, v35 op_sel:[0,0,1]
	v_cvt_pk_fp8_f32 v49, v38, v39 op_sel:[0,0,1]
	v_cvt_pk_fp8_f32 v50, v42, v43 op_sel:[0,0,1]
	v_cvt_pk_fp8_f32 v51, v46, v47 op_sel:[0,0,1]
	v_lshlrev_b64 v[32:33], 10, v[180:181]
	v_lshl_add_u64 v[32:33], s[6:7], 0, v[32:33]
	v_lshl_add_u64 v[32:33], v[32:33], 0, v[136:137]
	global_store_dwordx4 v[32:33], v[48:51], off
.LBB0_1082:
	s_or_b64 exec, exec, s[36:37]
	v_cmp_gt_i32_e32 vcc, s52, v151
	s_and_saveexec_b64 s[36:37], vcc
	s_cbranch_execz .LBB0_1084
	v_mov_b32_e32 v32, 0
	v_mov_b32_e32 v33, 0
	v_mov_b32_e32 v34, 0
	v_mov_b32_e32 v35, 0
	v_ashrrev_i32_e32 v185, 31, v184
	v_mul_f32_e32 v186, 0x41800000, v186
	v_pk_mul_f32 v[16:17], v[16:17], v[186:187] op_sel_hi:[1,0]
	v_pk_mul_f32 v[20:21], v[20:21], v[186:187] op_sel_hi:[1,0]
	v_pk_mul_f32 v[24:25], v[24:25], v[186:187] op_sel_hi:[1,0]
	v_pk_mul_f32 v[28:29], v[28:29], v[186:187] op_sel_hi:[1,0]
	v_cvt_pk_fp8_f32 v32, v16, v17
	v_cvt_pk_fp8_f32 v33, v20, v21
	v_cvt_pk_fp8_f32 v34, v24, v25
	v_cvt_pk_fp8_f32 v35, v28, v29
	v_pk_mul_f32 v[18:19], v[18:19], v[186:187] op_sel_hi:[1,0]
	v_pk_mul_f32 v[22:23], v[22:23], v[186:187] op_sel_hi:[1,0]
	v_pk_mul_f32 v[26:27], v[26:27], v[186:187] op_sel_hi:[1,0]
	v_pk_mul_f32 v[30:31], v[30:31], v[186:187] op_sel_hi:[1,0]
	v_cvt_pk_fp8_f32 v32, v18, v19 op_sel:[0,0,1]
	v_cvt_pk_fp8_f32 v33, v22, v23 op_sel:[0,0,1]
	v_cvt_pk_fp8_f32 v34, v26, v27 op_sel:[0,0,1]
	v_cvt_pk_fp8_f32 v35, v30, v31 op_sel:[0,0,1]
	v_lshlrev_b64 v[16:17], 10, v[184:185]
	v_lshl_add_u64 v[16:17], s[6:7], 0, v[16:17]
	v_lshl_add_u64 v[16:17], v[16:17], 0, v[136:137]
	global_store_dwordx4 v[16:17], v[32:35], off
.LBB0_1084:
	s_or_b64 exec, exec, s[36:37]
	v_cmp_gt_i32_e32 vcc, s52, v141
	s_and_saveexec_b64 s[36:37], vcc
	s_cbranch_execz .LBB0_1086
	v_mov_b32_e32 v16, 0
	v_mov_b32_e32 v17, 0
	v_mov_b32_e32 v18, 0
	v_mov_b32_e32 v19, 0
	v_ashrrev_i32_e32 v189, 31, v188
	v_mul_f32_e32 v190, 0x41800000, v190
	v_pk_mul_f32 v[0:1], v[0:1], v[190:191] op_sel_hi:[1,0]
	v_pk_mul_f32 v[4:5], v[4:5], v[190:191] op_sel_hi:[1,0]
	v_pk_mul_f32 v[8:9], v[8:9], v[190:191] op_sel_hi:[1,0]
	v_pk_mul_f32 v[12:13], v[12:13], v[190:191] op_sel_hi:[1,0]
	v_cvt_pk_fp8_f32 v16, v0, v1
	v_cvt_pk_fp8_f32 v17, v4, v5
	v_cvt_pk_fp8_f32 v18, v8, v9
	v_cvt_pk_fp8_f32 v19, v12, v13
	v_pk_mul_f32 v[2:3], v[2:3], v[190:191] op_sel_hi:[1,0]
	v_pk_mul_f32 v[6:7], v[6:7], v[190:191] op_sel_hi:[1,0]
	v_pk_mul_f32 v[10:11], v[10:11], v[190:191] op_sel_hi:[1,0]
	v_pk_mul_f32 v[14:15], v[14:15], v[190:191] op_sel_hi:[1,0]
	v_cvt_pk_fp8_f32 v16, v2, v3 op_sel:[0,0,1]
	v_cvt_pk_fp8_f32 v17, v6, v7 op_sel:[0,0,1]
	v_cvt_pk_fp8_f32 v18, v10, v11 op_sel:[0,0,1]
	v_cvt_pk_fp8_f32 v19, v14, v15 op_sel:[0,0,1]
	v_lshlrev_b64 v[0:1], 10, v[188:189]
	v_lshl_add_u64 v[0:1], s[6:7], 0, v[0:1]
	v_lshl_add_u64 v[0:1], v[0:1], 0, v[136:137]
	global_store_dwordx4 v[0:1], v[16:19], off

.LBB0_4461:
	v_lshl_or_b32 v136, s66, 8, v148
	v_ashrrev_i32_e32 v137, 31, v136
	v_add_u32_e32 v192, s48, v138
	v_ashrrev_i32_e32 v193, 31, v192
	v_lshlrev_b64 v[192:193], 2, v[192:193]
	v_lshl_add_u64 v[194:195], s[12:13], 0, v[192:193]
	v_lshl_add_u64 v[192:193], s[8:9], 0, v[192:193]
	global_load_dword v160, v[192:193], off
	global_load_dword v162, v[194:195], off
	global_load_dword v164, v[192:193], off offset:64
	global_load_dword v166, v[194:195], off offset:64
	global_load_dword v168, v[192:193], off offset:128
	global_load_dword v170, v[194:195], off offset:128
	global_load_dword v172, v[192:193], off offset:192
	global_load_dword v174, v[194:195], off offset:192
	global_load_dword v176, v[192:193], off offset:512
	global_load_dword v178, v[194:195], off offset:512
	global_load_dword v180, v[192:193], off offset:576
	global_load_dword v182, v[194:195], off offset:576
	global_load_dword v184, v[192:193], off offset:640
	global_load_dword v186, v[194:195], off offset:640
	global_load_dword v188, v[192:193], off offset:704
	global_load_dword v190, v[194:195], off offset:704
	s_waitcnt vmcnt(0)
	v_cmp_gt_i32_e32 vcc, s51, v138
	s_and_saveexec_b64 s[36:37], vcc
	s_cbranch_execz .LBB0_4463
	v_mov_b32_e32 v152, 0
	v_mov_b32_e32 v153, 0
	v_mov_b32_e32 v154, 0
	v_mov_b32_e32 v155, 0
	v_ashrrev_i32_e32 v161, 31, v160
	v_mul_f32_e32 v162, 0x41800000, v162
	v_pk_mul_f32 v[112:113], v[112:113], v[162:163] op_sel_hi:[1,0]
	v_pk_mul_f32 v[116:117], v[116:117], v[162:163] op_sel_hi:[1,0]
	v_pk_mul_f32 v[120:121], v[120:121], v[162:163] op_sel_hi:[1,0]
	v_pk_mul_f32 v[124:125], v[124:125], v[162:163] op_sel_hi:[1,0]
	v_cvt_pk_fp8_f32 v152, v112, v113
	v_cvt_pk_fp8_f32 v153, v116, v117
	v_cvt_pk_fp8_f32 v154, v120, v121
	v_cvt_pk_fp8_f32 v155, v124, v125
	v_pk_mul_f32 v[114:115], v[114:115], v[162:163] op_sel_hi:[1,0]
	v_pk_mul_f32 v[118:119], v[118:119], v[162:163] op_sel_hi:[1,0]
	v_pk_mul_f32 v[122:123], v[122:123], v[162:163] op_sel_hi:[1,0]
	v_pk_mul_f32 v[126:127], v[126:127], v[162:163] op_sel_hi:[1,0]
	v_cvt_pk_fp8_f32 v152, v114, v115 op_sel:[0,0,1]
	v_cvt_pk_fp8_f32 v153, v118, v119 op_sel:[0,0,1]
	v_cvt_pk_fp8_f32 v154, v122, v123 op_sel:[0,0,1]
	v_cvt_pk_fp8_f32 v155, v126, v127 op_sel:[0,0,1]
	v_lshlrev_b64 v[112:113], 10, v[160:161]
	v_lshl_add_u64 v[112:113], s[6:7], 0, v[112:113]
	v_lshl_add_u64 v[112:113], v[112:113], 0, v[136:137]
	global_store_dwordx4 v[112:113], v[152:155], off
.LBB0_4463:
	s_or_b64 exec, exec, s[36:37]
	v_or_b32_e32 v112, 16, v138
	v_cmp_gt_i32_e32 vcc, s51, v112
	s_and_saveexec_b64 s[36:37], vcc
	s_cbranch_execz .LBB0_4465
	v_mov_b32_e32 v112, 0
	v_mov_b32_e32 v113, 0
	v_mov_b32_e32 v114, 0
	v_mov_b32_e32 v115, 0
	v_ashrrev_i32_e32 v165, 31, v164
	v_mul_f32_e32 v166, 0x41800000, v166
	v_pk_mul_f32 v[96:97], v[96:97], v[166:167] op_sel_hi:[1,0]
	v_pk_mul_f32 v[100:101], v[100:101], v[166:167] op_sel_hi:[1,0]
	v_pk_mul_f32 v[104:105], v[104:105], v[166:167] op_sel_hi:[1,0]
	v_pk_mul_f32 v[108:109], v[108:109], v[166:167] op_sel_hi:[1,0]
	v_cvt_pk_fp8_f32 v112, v96, v97
	v_cvt_pk_fp8_f32 v113, v100, v101
	v_cvt_pk_fp8_f32 v114, v104, v105
	v_cvt_pk_fp8_f32 v115, v108, v109
	v_pk_mul_f32 v[98:99], v[98:99], v[166:167] op_sel_hi:[1,0]
	v_pk_mul_f32 v[102:103], v[102:103], v[166:167] op_sel_hi:[1,0]
	v_pk_mul_f32 v[106:107], v[106:107], v[166:167] op_sel_hi:[1,0]
	v_pk_mul_f32 v[110:111], v[110:111], v[166:167] op_sel_hi:[1,0]
	v_cvt_pk_fp8_f32 v112, v98, v99 op_sel:[0,0,1]
	v_cvt_pk_fp8_f32 v113, v102, v103 op_sel:[0,0,1]
	v_cvt_pk_fp8_f32 v114, v106, v107 op_sel:[0,0,1]
	v_cvt_pk_fp8_f32 v115, v110, v111 op_sel:[0,0,1]
	v_lshlrev_b64 v[96:97], 10, v[164:165]
	v_lshl_add_u64 v[96:97], s[6:7], 0, v[96:97]
	v_lshl_add_u64 v[96:97], v[96:97], 0, v[136:137]
	global_store_dwordx4 v[96:97], v[112:115], off
.LBB0_4465:
	s_or_b64 exec, exec, s[36:37]
	v_or_b32_e32 v96, 32, v138
	v_cmp_gt_i32_e32 vcc, s51, v96
	s_and_saveexec_b64 s[36:37], vcc
	s_cbranch_execz .LBB0_4467
	v_mov_b32_e32 v96, 0
	v_mov_b32_e32 v97, 0
	v_mov_b32_e32 v98, 0
	v_mov_b32_e32 v99, 0
	v_ashrrev_i32_e32 v169, 31, v168
	v_mul_f32_e32 v170, 0x41800000, v170
	v_pk_mul_f32 v[80:81], v[80:81], v[170:171] op_sel_hi:[1,0]
	v_pk_mul_f32 v[84:85], v[84:85], v[170:171] op_sel_hi:[1,0]
	v_pk_mul_f32 v[88:89], v[88:89], v[170:171] op_sel_hi:[1,0]
	v_pk_mul_f32 v[92:93], v[92:93], v[170:171] op_sel_hi:[1,0]
	v_cvt_pk_fp8_f32 v96, v80, v81
	v_cvt_pk_fp8_f32 v97, v84, v85
	v_cvt_pk_fp8_f32 v98, v88, v89
	v_cvt_pk_fp8_f32 v99, v92, v93
	v_pk_mul_f32 v[82:83], v[82:83], v[170:171] op_sel_hi:[1,0]
	v_pk_mul_f32 v[86:87], v[86:87], v[170:171] op_sel_hi:[1,0]
	v_pk_mul_f32 v[90:91], v[90:91], v[170:171] op_sel_hi:[1,0]
	v_pk_mul_f32 v[94:95], v[94:95], v[170:171] op_sel_hi:[1,0]
	v_cvt_pk_fp8_f32 v96, v82, v83 op_sel:[0,0,1]
	v_cvt_pk_fp8_f32 v97, v86, v87 op_sel:[0,0,1]
	v_cvt_pk_fp8_f32 v98, v90, v91 op_sel:[0,0,1]
	v_cvt_pk_fp8_f32 v99, v94, v95 op_sel:[0,0,1]
	v_lshlrev_b64 v[80:81], 10, v[168:169]
	v_lshl_add_u64 v[80:81], s[6:7], 0, v[80:81]
	v_lshl_add_u64 v[80:81], v[80:81], 0, v[136:137]
	global_store_dwordx4 v[80:81], v[96:99], off
.LBB0_4467:
	s_or_b64 exec, exec, s[36:37]
	v_or_b32_e32 v80, 48, v138
	v_cmp_gt_i32_e32 vcc, s51, v80
	s_and_saveexec_b64 s[36:37], vcc
	s_cbranch_execz .LBB0_4469
	v_mov_b32_e32 v80, 0
	v_mov_b32_e32 v81, 0
	v_mov_b32_e32 v82, 0
	v_mov_b32_e32 v83, 0
	v_ashrrev_i32_e32 v173, 31, v172
	v_mul_f32_e32 v174, 0x41800000, v174
	v_pk_mul_f32 v[64:65], v[64:65], v[174:175] op_sel_hi:[1,0]
	v_pk_mul_f32 v[68:69], v[68:69], v[174:175] op_sel_hi:[1,0]
	v_pk_mul_f32 v[72:73], v[72:73], v[174:175] op_sel_hi:[1,0]
	v_pk_mul_f32 v[76:77], v[76:77], v[174:175] op_sel_hi:[1,0]
	v_cvt_pk_fp8_f32 v80, v64, v65
	v_cvt_pk_fp8_f32 v81, v68, v69
	v_cvt_pk_fp8_f32 v82, v72, v73
	v_cvt_pk_fp8_f32 v83, v76, v77
	v_pk_mul_f32 v[66:67], v[66:67], v[174:175] op_sel_hi:[1,0]
	v_pk_mul_f32 v[70:71], v[70:71], v[174:175] op_sel_hi:[1,0]
	v_pk_mul_f32 v[74:75], v[74:75], v[174:175] op_sel_hi:[1,0]
	v_pk_mul_f32 v[78:79], v[78:79], v[174:175] op_sel_hi:[1,0]
	v_cvt_pk_fp8_f32 v80, v66, v67 op_sel:[0,0,1]
	v_cvt_pk_fp8_f32 v81, v70, v71 op_sel:[0,0,1]
	v_cvt_pk_fp8_f32 v82, v74, v75 op_sel:[0,0,1]
	v_cvt_pk_fp8_f32 v83, v78, v79 op_sel:[0,0,1]
	v_lshlrev_b64 v[64:65], 10, v[172:173]
	v_lshl_add_u64 v[64:65], s[6:7], 0, v[64:65]
	v_lshl_add_u64 v[64:65], v[64:65], 0, v[136:137]
	global_store_dwordx4 v[64:65], v[80:83], off
.LBB0_4469:
	s_or_b64 exec, exec, s[36:37]
	v_add_u32_e32 v64, 0x80, v138
	v_cmp_gt_i32_e32 vcc, s51, v64
	s_and_saveexec_b64 s[36:37], vcc
	s_cbranch_execz .LBB0_4471
	v_mov_b32_e32 v64, 0
	v_mov_b32_e32 v65, 0
	v_mov_b32_e32 v66, 0
	v_mov_b32_e32 v67, 0
	v_ashrrev_i32_e32 v177, 31, v176
	v_mul_f32_e32 v178, 0x41800000, v178
	v_pk_mul_f32 v[48:49], v[48:49], v[178:179] op_sel_hi:[1,0]
	v_pk_mul_f32 v[52:53], v[52:53], v[178:179] op_sel_hi:[1,0]
	v_pk_mul_f32 v[56:57], v[56:57], v[178:179] op_sel_hi:[1,0]
	v_pk_mul_f32 v[60:61], v[60:61], v[178:179] op_sel_hi:[1,0]
	v_cvt_pk_fp8_f32 v64, v48, v49
	v_cvt_pk_fp8_f32 v65, v52, v53
	v_cvt_pk_fp8_f32 v66, v56, v57
	v_cvt_pk_fp8_f32 v67, v60, v61
	v_pk_mul_f32 v[50:51], v[50:51], v[178:179] op_sel_hi:[1,0]
	v_pk_mul_f32 v[54:55], v[54:55], v[178:179] op_sel_hi:[1,0]
	v_pk_mul_f32 v[58:59], v[58:59], v[178:179] op_sel_hi:[1,0]
	v_pk_mul_f32 v[62:63], v[62:63], v[178:179] op_sel_hi:[1,0]
	v_cvt_pk_fp8_f32 v64, v50, v51 op_sel:[0,0,1]
	v_cvt_pk_fp8_f32 v65, v54, v55 op_sel:[0,0,1]
	v_cvt_pk_fp8_f32 v66, v58, v59 op_sel:[0,0,1]
	v_cvt_pk_fp8_f32 v67, v62, v63 op_sel:[0,0,1]
	v_lshlrev_b64 v[48:49], 10, v[176:177]
	v_lshl_add_u64 v[48:49], s[6:7], 0, v[48:49]
	v_lshl_add_u64 v[48:49], v[48:49], 0, v[136:137]
	global_store_dwordx4 v[48:49], v[64:67], off
.LBB0_4471:
	s_or_b64 exec, exec, s[36:37]
	v_add_u32_e32 v48, 0x90, v138
	v_cmp_gt_i32_e32 vcc, s51, v48
	s_and_saveexec_b64 s[36:37], vcc
	s_cbranch_execz .LBB0_4473
	v_mov_b32_e32 v48, 0
	v_mov_b32_e32 v49, 0
	v_mov_b32_e32 v50, 0
	v_mov_b32_e32 v51, 0
	v_ashrrev_i32_e32 v181, 31, v180
	v_mul_f32_e32 v182, 0x41800000, v182
	v_pk_mul_f32 v[32:33], v[32:33], v[182:183] op_sel_hi:[1,0]
	v_pk_mul_f32 v[36:37], v[36:37], v[182:183] op_sel_hi:[1,0]
	v_pk_mul_f32 v[40:41], v[40:41], v[182:183] op_sel_hi:[1,0]
	v_pk_mul_f32 v[44:45], v[44:45], v[182:183] op_sel_hi:[1,0]
	v_cvt_pk_fp8_f32 v48, v32, v33
	v_cvt_pk_fp8_f32 v49, v36, v37
	v_cvt_pk_fp8_f32 v50, v40, v41
	v_cvt_pk_fp8_f32 v51, v44, v45
	v_pk_mul_f32 v[34:35], v[34:35], v[182:183] op_sel_hi:[1,0]
	v_pk_mul_f32 v[38:39], v[38:39], v[182:183] op_sel_hi:[1,0]
	v_pk_mul_f32 v[42:43], v[42:43], v[182:183] op_sel_hi:[1,0]
	v_pk_mul_f32 v[46:47], v[46:47], v[182:183] op_sel_hi:[1,0]
	v_cvt_pk_fp8_f32 v48, v34, v35 op_sel:[0,0,1]
	v_cvt_pk_fp8_f32 v49, v38, v39 op_sel:[0,0,1]
	v_cvt_pk_fp8_f32 v50, v42, v43 op_sel:[0,0,1]
	v_cvt_pk_fp8_f32 v51, v46, v47 op_sel:[0,0,1]
	v_lshlrev_b64 v[32:33], 10, v[180:181]
	v_lshl_add_u64 v[32:33], s[6:7], 0, v[32:33]
	v_lshl_add_u64 v[32:33], v[32:33], 0, v[136:137]
	global_store_dwordx4 v[32:33], v[48:51], off
.LBB0_4473:
	s_or_b64 exec, exec, s[36:37]
	v_cmp_gt_i32_e32 vcc, s51, v151
	s_and_saveexec_b64 s[36:37], vcc
	s_cbranch_execz .LBB0_4475
	v_mov_b32_e32 v32, 0
	v_mov_b32_e32 v33, 0
	v_mov_b32_e32 v34, 0
	v_mov_b32_e32 v35, 0
	v_ashrrev_i32_e32 v185, 31, v184
	v_mul_f32_e32 v186, 0x41800000, v186
	v_pk_mul_f32 v[16:17], v[16:17], v[186:187] op_sel_hi:[1,0]
	v_pk_mul_f32 v[20:21], v[20:21], v[186:187] op_sel_hi:[1,0]
	v_pk_mul_f32 v[24:25], v[24:25], v[186:187] op_sel_hi:[1,0]
	v_pk_mul_f32 v[28:29], v[28:29], v[186:187] op_sel_hi:[1,0]
	v_cvt_pk_fp8_f32 v32, v16, v17
	v_cvt_pk_fp8_f32 v33, v20, v21
	v_cvt_pk_fp8_f32 v34, v24, v25
	v_cvt_pk_fp8_f32 v35, v28, v29
	v_pk_mul_f32 v[18:19], v[18:19], v[186:187] op_sel_hi:[1,0]
	v_pk_mul_f32 v[22:23], v[22:23], v[186:187] op_sel_hi:[1,0]
	v_pk_mul_f32 v[26:27], v[26:27], v[186:187] op_sel_hi:[1,0]
	v_pk_mul_f32 v[30:31], v[30:31], v[186:187] op_sel_hi:[1,0]
	v_cvt_pk_fp8_f32 v32, v18, v19 op_sel:[0,0,1]
	v_cvt_pk_fp8_f32 v33, v22, v23 op_sel:[0,0,1]
	v_cvt_pk_fp8_f32 v34, v26, v27 op_sel:[0,0,1]
	v_cvt_pk_fp8_f32 v35, v30, v31 op_sel:[0,0,1]
	v_lshlrev_b64 v[16:17], 10, v[184:185]
	v_lshl_add_u64 v[16:17], s[6:7], 0, v[16:17]
	v_lshl_add_u64 v[16:17], v[16:17], 0, v[136:137]
	global_store_dwordx4 v[16:17], v[32:35], off
.LBB0_4475:
	s_or_b64 exec, exec, s[36:37]
	v_cmp_gt_i32_e32 vcc, s51, v141
	s_and_saveexec_b64 s[36:37], vcc
	s_cbranch_execz .LBB0_4477
	v_mov_b32_e32 v16, 0
	v_mov_b32_e32 v17, 0
	v_mov_b32_e32 v18, 0
	v_mov_b32_e32 v19, 0
	v_ashrrev_i32_e32 v189, 31, v188
	v_mul_f32_e32 v190, 0x41800000, v190
	v_pk_mul_f32 v[0:1], v[0:1], v[190:191] op_sel_hi:[1,0]
	v_pk_mul_f32 v[4:5], v[4:5], v[190:191] op_sel_hi:[1,0]
	v_pk_mul_f32 v[8:9], v[8:9], v[190:191] op_sel_hi:[1,0]
	v_pk_mul_f32 v[12:13], v[12:13], v[190:191] op_sel_hi:[1,0]
	v_cvt_pk_fp8_f32 v16, v0, v1
	v_cvt_pk_fp8_f32 v17, v4, v5
	v_cvt_pk_fp8_f32 v18, v8, v9
	v_cvt_pk_fp8_f32 v19, v12, v13
	v_pk_mul_f32 v[2:3], v[2:3], v[190:191] op_sel_hi:[1,0]
	v_pk_mul_f32 v[6:7], v[6:7], v[190:191] op_sel_hi:[1,0]
	v_pk_mul_f32 v[10:11], v[10:11], v[190:191] op_sel_hi:[1,0]
	v_pk_mul_f32 v[14:15], v[14:15], v[190:191] op_sel_hi:[1,0]
	v_cvt_pk_fp8_f32 v16, v2, v3 op_sel:[0,0,1]
	v_cvt_pk_fp8_f32 v17, v6, v7 op_sel:[0,0,1]
	v_cvt_pk_fp8_f32 v18, v10, v11 op_sel:[0,0,1]
	v_cvt_pk_fp8_f32 v19, v14, v15 op_sel:[0,0,1]
	v_lshlrev_b64 v[0:1], 10, v[188:189]
	v_lshl_add_u64 v[0:1], s[6:7], 0, v[0:1]
	v_lshl_add_u64 v[0:1], v[0:1], 0, v[136:137]
	global_store_dwordx4 v[0:1], v[16:19], off
